# baseline (speedup 1.0000x reference)
.LBB3_83:
	v_add_u32_e32 v82, s18, v115
	v_add_u32_e32 v118, 0x5000, v82
	v_or_b32_e32 v115, v118, v116
	v_add_u32_e32 v124, 0, v115
	ds_read_b128 v[86:89], v124 offset:53248
	ds_read_b128 v[90:93], v124 offset:55296
	ds_read_b128 v[82:85], v136 offset:53248
	ds_read_b128 v[138:141], v136 offset:55296
	s_and_b64 vcc, exec, s[4:5]
	s_waitcnt lgkmcnt(0)
	v_mfma_f32_16x16x32_f16 v[18:21], v[86:89], v[82:85], v[18:21]
	s_mov_b32 m0, s76
	v_mfma_f32_16x16x32_f16 v[22:25], v[90:93], v[82:85], v[22:25]
	global_load_lds_dwordx4 v168, s[72:73]
	v_mfma_f32_16x16x32_f16 v[26:29], v[86:89], v[138:141], v[26:29]
	s_mov_b32 m0, s77
	v_mfma_f32_16x16x32_f16 v[30:33], v[90:93], v[138:141], v[30:33]
	global_load_lds_dwordx4 v169, s[72:73]
	ds_read_b128 v[82:85], v136 offset:57344
	ds_read_b128 v[138:141], v136 offset:59392
	s_waitcnt lgkmcnt(0)
	v_mfma_f32_16x16x32_f16 v[34:37], v[86:89], v[82:85], v[34:37]
	s_mov_b32 m0, s78
	v_mfma_f32_16x16x32_f16 v[38:41], v[90:93], v[82:85], v[38:41]
	global_load_lds_dwordx4 v170, s[72:73]
	v_mfma_f32_16x16x32_f16 v[42:45], v[86:89], v[138:141], v[42:45]
	s_mov_b32 m0, s79
	v_mfma_f32_16x16x32_f16 v[46:49], v[90:93], v[138:141], v[46:49]
	global_load_lds_dwordx4 v171, s[72:73]
	ds_read_b128 v[82:85], v136 offset:61440
	ds_read_b128 v[140:143], v136 offset:63488
	v_add_u32_e32 v138, 0xd000, v136
	s_waitcnt lgkmcnt(0)
	ds_read_b128 v[176:179], v138 offset:16384
	ds_read_b128 v[180:183], v138 offset:18432
	v_mfma_f32_16x16x32_f16 v[50:53], v[86:89], v[82:85], v[50:53]
	s_mov_b32 m0, s80
	v_mfma_f32_16x16x32_f16 v[54:57], v[90:93], v[82:85], v[54:57]
	global_load_lds_dwordx4 v172, s[74:75]
	v_mfma_f32_16x16x32_f16 v[62:65], v[86:89], v[140:143], v[62:65]
	s_mov_b32 m0, s81
	v_mfma_f32_16x16x32_f16 v[82:85], v[90:93], v[140:143], v[58:61]
	global_load_lds_dwordx4 v173, s[74:75]
	s_nop 2
	ds_read_b128 v[58:61], v138 offset:12288
	ds_read_b128 v[140:143], v138 offset:14336
	s_waitcnt lgkmcnt(0)
	v_mfma_f32_16x16x32_f16 v[66:69], v[86:89], v[58:61], v[66:69]
	v_mfma_f32_16x16x32_f16 v[70:73], v[90:93], v[58:61], v[70:73]
	v_mfma_f32_16x16x32_f16 v[74:77], v[86:89], v[140:143], v[74:77]
	v_mfma_f32_16x16x32_f16 v[78:81], v[90:93], v[140:143], v[78:81]
	s_cbranch_vccnz .LBB3_85
	s_waitcnt lgkmcnt(1)
	v_mfma_f32_16x16x32_f16 v[10:13], v[86:89], v[176:179], v[10:13]
	v_mfma_f32_16x16x32_f16 v[14:17], v[90:93], v[176:179], v[14:17]
.LBB3_85:
	s_and_b64 vcc, exec, s[6:7]
	s_cbranch_vccnz .LBB3_87
	s_waitcnt lgkmcnt(0)
	v_mfma_f32_16x16x32_f16 v[2:5], v[86:89], v[180:183], v[2:5]
	v_mfma_f32_16x16x32_f16 v[6:9], v[90:93], v[180:183], v[6:9]

.LBB3_94:
	s_and_b64 vcc, exec, s[4:5]
	s_waitcnt lgkmcnt(5)
	v_mfma_f32_16x16x32_f16 v[22:25], v[86:89], v[118:121], v[22:25]
	s_mov_b32 m0, s82
	v_mfma_f32_16x16x32_f16 v[18:21], v[82:85], v[118:121], v[18:21]
	global_load_lds_dwordx4 v168, s[72:73]
	s_waitcnt lgkmcnt(4)
	v_mfma_f32_16x16x32_f16 v[26:29], v[82:85], v[142:145], v[26:29]
	s_mov_b32 m0, s83
	v_mfma_f32_16x16x32_f16 v[30:33], v[86:89], v[142:145], v[30:33]
	global_load_lds_dwordx4 v169, s[72:73]
	s_waitcnt lgkmcnt(3)
	v_mfma_f32_16x16x32_f16 v[34:37], v[82:85], v[148:151], v[34:37]
	s_mov_b32 m0, s84
	v_mfma_f32_16x16x32_f16 v[38:41], v[86:89], v[148:151], v[38:41]
	global_load_lds_dwordx4 v170, s[72:73]
	ds_read_b128 v[148:151], v125 offset:12288
	s_waitcnt lgkmcnt(3)
	v_mfma_f32_16x16x32_f16 v[42:45], v[82:85], v[152:155], v[42:45]
	s_mov_b32 m0, s85
	v_mfma_f32_16x16x32_f16 v[46:49], v[86:89], v[152:155], v[46:49]
	global_load_lds_dwordx4 v171, s[72:73]
	ds_read_b128 v[152:155], v125 offset:14336
	s_waitcnt lgkmcnt(3)
	ds_read_b128 v[176:179], v125 offset:16384
	ds_read_b128 v[180:183], v125 offset:18432
	v_mfma_f32_16x16x32_f16 v[50:53], v[82:85], v[156:159], v[50:53]
	s_mov_b32 m0, s86
	v_mfma_f32_16x16x32_f16 v[54:57], v[86:89], v[156:159], v[54:57]
	global_load_lds_dwordx4 v172, s[74:75]
	s_waitcnt lgkmcnt(4)
	v_mfma_f32_16x16x32_f16 v[58:61], v[82:85], v[160:163], v[58:61]
	s_mov_b32 m0, s87
	v_mfma_f32_16x16x32_f16 v[62:65], v[86:89], v[160:163], v[62:65]
	global_load_lds_dwordx4 v173, s[74:75]
	s_waitcnt lgkmcnt(3)
	v_mfma_f32_16x16x32_f16 v[66:69], v[82:85], v[148:151], v[66:69]
	v_mfma_f32_16x16x32_f16 v[70:73], v[86:89], v[148:151], v[70:73]
	s_waitcnt lgkmcnt(2)
	v_mfma_f32_16x16x32_f16 v[74:77], v[82:85], v[152:155], v[74:77]
	v_mfma_f32_16x16x32_f16 v[78:81], v[86:89], v[152:155], v[78:81]
	s_cbranch_vccnz .LBB3_96
	s_waitcnt lgkmcnt(1)
	v_mfma_f32_16x16x32_f16 v[10:13], v[82:85], v[176:179], v[10:13]
	v_mfma_f32_16x16x32_f16 v[14:17], v[86:89], v[176:179], v[14:17]
.LBB3_96:
	s_and_b64 vcc, exec, s[6:7]
	s_cbranch_vccnz .LBB3_98
	s_waitcnt lgkmcnt(0)
	v_mfma_f32_16x16x32_f16 v[2:5], v[82:85], v[180:183], v[2:5]
	v_mfma_f32_16x16x32_f16 v[6:9], v[86:89], v[180:183], v[6:9]
.LBB3_98:
	s_waitcnt lgkmcnt(0)
	v_add_u32_e32 v142, s17, v116
	ds_read_b128 v[82:85], v142
	ds_read_b128 v[86:89], v142 offset:2048
	v_add_u32_e32 v141, s17, v114
	ds_read_b128 v[114:117], v141
	ds_read_b128 v[118:121], v141 offset:2048
	ds_read_b128 v[148:151], v141 offset:4096
	ds_read_b128 v[152:155], v141 offset:6144
	ds_read_b128 v[156:159], v141 offset:8192
	ds_read_b128 v[160:163], v141 offset:10240
	s_and_b64 vcc, exec, s[4:5]
	s_waitcnt lgkmcnt(5)
	v_mfma_f32_16x16x32_f16 v[22:25], v[86:89], v[114:117], v[22:25]
	v_mfma_f32_16x16x32_f16 v[18:21], v[82:85], v[114:117], v[18:21]
	s_waitcnt lgkmcnt(4)
	v_mfma_f32_16x16x32_f16 v[26:29], v[82:85], v[118:121], v[26:29]
	v_mfma_f32_16x16x32_f16 v[30:33], v[86:89], v[118:121], v[30:33]
	s_waitcnt lgkmcnt(3)
	v_mfma_f32_16x16x32_f16 v[34:37], v[82:85], v[148:151], v[34:37]
	v_mfma_f32_16x16x32_f16 v[38:41], v[86:89], v[148:151], v[38:41]
	ds_read_b128 v[148:151], v141 offset:12288
	s_waitcnt lgkmcnt(3)
	v_mfma_f32_16x16x32_f16 v[42:45], v[82:85], v[152:155], v[42:45]
	v_mfma_f32_16x16x32_f16 v[46:49], v[86:89], v[152:155], v[46:49]
	ds_read_b128 v[152:155], v141 offset:14336
	s_waitcnt lgkmcnt(3)
	ds_read_b128 v[176:179], v141 offset:16384
	ds_read_b128 v[180:183], v141 offset:18432
	v_mfma_f32_16x16x32_f16 v[50:53], v[82:85], v[156:159], v[50:53]
	v_mfma_f32_16x16x32_f16 v[54:57], v[86:89], v[156:159], v[54:57]
	s_waitcnt lgkmcnt(4)
	v_mfma_f32_16x16x32_f16 v[58:61], v[82:85], v[160:163], v[58:61]
	v_mfma_f32_16x16x32_f16 v[62:65], v[86:89], v[160:163], v[62:65]
	s_waitcnt lgkmcnt(3)
	v_mfma_f32_16x16x32_f16 v[66:69], v[82:85], v[148:151], v[66:69]
	v_mfma_f32_16x16x32_f16 v[70:73], v[86:89], v[148:151], v[70:73]
	s_waitcnt lgkmcnt(2)
	v_mfma_f32_16x16x32_f16 v[74:77], v[82:85], v[152:155], v[74:77]
	v_mfma_f32_16x16x32_f16 v[78:81], v[86:89], v[152:155], v[78:81]
	s_cbranch_vccnz .LBB3_100
	s_waitcnt lgkmcnt(1)
	v_mfma_f32_16x16x32_f16 v[10:13], v[82:85], v[176:179], v[10:13]
	v_mfma_f32_16x16x32_f16 v[14:17], v[86:89], v[176:179], v[14:17]

.LBB3_108:
	s_waitcnt lgkmcnt(0)
	ds_read_b128 v[82:85], v122 offset:20480
	ds_read_b128 v[86:89], v122 offset:22528
	ds_read_b128 v[112:115], v136
	ds_read_b128 v[116:119], v136 offset:2048
	ds_read_b128 v[148:151], v136 offset:4096
	ds_read_b128 v[152:155], v136 offset:6144
	ds_read_b128 v[156:159], v136 offset:8192
	ds_read_b128 v[160:163], v136 offset:10240
	s_and_b64 vcc, exec, s[4:5]
	s_waitcnt lgkmcnt(5)
	v_mfma_f32_16x16x32_f16 v[18:21], v[82:85], v[112:115], v[18:21]
	s_mov_b32 m0, s88
	v_mfma_f32_16x16x32_f16 v[22:25], v[86:89], v[112:115], v[22:25]
	global_load_lds_dwordx4 v168, s[72:73]
	s_waitcnt lgkmcnt(4)
	v_mfma_f32_16x16x32_f16 v[26:29], v[82:85], v[116:119], v[26:29]
	s_mov_b32 m0, s89
	v_mfma_f32_16x16x32_f16 v[30:33], v[86:89], v[116:119], v[30:33]
	global_load_lds_dwordx4 v169, s[72:73]
	s_waitcnt lgkmcnt(3)
	v_mfma_f32_16x16x32_f16 v[34:37], v[82:85], v[148:151], v[34:37]
	s_mov_b32 m0, s90
	v_mfma_f32_16x16x32_f16 v[38:41], v[86:89], v[148:151], v[38:41]
	global_load_lds_dwordx4 v170, s[72:73]
	ds_read_b128 v[148:151], v136 offset:12288
	s_waitcnt lgkmcnt(3)
	v_mfma_f32_16x16x32_f16 v[42:45], v[82:85], v[152:155], v[42:45]
	s_mov_b32 m0, s91
	v_mfma_f32_16x16x32_f16 v[46:49], v[86:89], v[152:155], v[46:49]
	global_load_lds_dwordx4 v171, s[72:73]
	ds_read_b128 v[152:155], v136 offset:14336
	s_waitcnt lgkmcnt(3)
	ds_read_b128 v[176:179], v136 offset:16384
	ds_read_b128 v[180:183], v136 offset:18432
	v_mfma_f32_16x16x32_f16 v[50:53], v[82:85], v[156:159], v[50:53]
	s_mov_b32 m0, s92
	v_mfma_f32_16x16x32_f16 v[54:57], v[86:89], v[156:159], v[54:57]
	global_load_lds_dwordx4 v172, s[74:75]
	s_waitcnt lgkmcnt(4)
	v_mfma_f32_16x16x32_f16 v[58:61], v[82:85], v[160:163], v[58:61]
	s_mov_b32 m0, s93
	v_mfma_f32_16x16x32_f16 v[62:65], v[86:89], v[160:163], v[62:65]
	global_load_lds_dwordx4 v173, s[74:75]
	s_waitcnt lgkmcnt(3)
	v_mfma_f32_16x16x32_f16 v[66:69], v[82:85], v[148:151], v[66:69]
	v_mfma_f32_16x16x32_f16 v[70:73], v[86:89], v[148:151], v[70:73]
	s_waitcnt lgkmcnt(2)
	v_mfma_f32_16x16x32_f16 v[74:77], v[82:85], v[152:155], v[74:77]
	v_mfma_f32_16x16x32_f16 v[78:81], v[86:89], v[152:155], v[78:81]
	s_cbranch_vccnz .LBB3_110
	s_waitcnt lgkmcnt(1)
	v_mfma_f32_16x16x32_f16 v[10:13], v[82:85], v[176:179], v[10:13]
	v_mfma_f32_16x16x32_f16 v[14:17], v[86:89], v[176:179], v[14:17]

.LBB3_119:
	s_and_b64 vcc, exec, s[4:5]
	s_waitcnt lgkmcnt(5)
	v_mfma_f32_16x16x32_f16 v[18:21], v[82:85], v[112:115], v[18:21]
	s_mov_b32 m0, s76
	v_mfma_f32_16x16x32_f16 v[22:25], v[86:89], v[112:115], v[22:25]
	global_load_lds_dwordx4 v168, s[72:73]
	s_waitcnt lgkmcnt(4)
	v_mfma_f32_16x16x32_f16 v[26:29], v[82:85], v[116:119], v[26:29]
	s_mov_b32 m0, s77
	v_mfma_f32_16x16x32_f16 v[30:33], v[86:89], v[116:119], v[30:33]
	global_load_lds_dwordx4 v169, s[72:73]
	s_waitcnt lgkmcnt(3)
	v_mfma_f32_16x16x32_f16 v[34:37], v[82:85], v[148:151], v[34:37]
	s_mov_b32 m0, s78
	v_mfma_f32_16x16x32_f16 v[38:41], v[86:89], v[148:151], v[38:41]
	global_load_lds_dwordx4 v170, s[72:73]
	ds_read_b128 v[148:151], v138 offset:12288
	s_waitcnt lgkmcnt(3)
	v_mfma_f32_16x16x32_f16 v[42:45], v[82:85], v[152:155], v[42:45]
	s_mov_b32 m0, s79
	v_mfma_f32_16x16x32_f16 v[46:49], v[86:89], v[152:155], v[46:49]
	global_load_lds_dwordx4 v171, s[72:73]
	ds_read_b128 v[152:155], v138 offset:14336
	s_waitcnt lgkmcnt(3)
	ds_read_b128 v[176:179], v138 offset:16384
	ds_read_b128 v[180:183], v138 offset:18432
	v_mfma_f32_16x16x32_f16 v[50:53], v[82:85], v[156:159], v[50:53]
	s_mov_b32 m0, s80
	v_mfma_f32_16x16x32_f16 v[54:57], v[86:89], v[156:159], v[54:57]
	global_load_lds_dwordx4 v172, s[74:75]
	s_waitcnt lgkmcnt(4)
	v_mfma_f32_16x16x32_f16 v[58:61], v[82:85], v[160:163], v[58:61]
	s_mov_b32 m0, s81
	v_mfma_f32_16x16x32_f16 v[62:65], v[86:89], v[160:163], v[62:65]
	global_load_lds_dwordx4 v173, s[74:75]
	s_waitcnt lgkmcnt(3)
	v_mfma_f32_16x16x32_f16 v[66:69], v[82:85], v[148:151], v[66:69]
	v_mfma_f32_16x16x32_f16 v[70:73], v[86:89], v[148:151], v[70:73]
	s_waitcnt lgkmcnt(2)
	v_mfma_f32_16x16x32_f16 v[74:77], v[82:85], v[152:155], v[74:77]
	v_mfma_f32_16x16x32_f16 v[78:81], v[86:89], v[152:155], v[78:81]
	s_cbranch_vccnz .LBB3_121
	s_waitcnt lgkmcnt(1)
	v_mfma_f32_16x16x32_f16 v[10:13], v[82:85], v[176:179], v[10:13]
	v_mfma_f32_16x16x32_f16 v[14:17], v[86:89], v[176:179], v[14:17]

.LBB3_130:
	s_and_b64 vcc, exec, s[4:5]
	s_waitcnt lgkmcnt(5)
	v_mfma_f32_16x16x32_f16 v[18:21], v[114:117], v[82:85], v[18:21]
	s_mov_b32 m0, s82
	v_mfma_f32_16x16x32_f16 v[22:25], v[118:121], v[82:85], v[22:25]
	global_load_lds_dwordx4 v168, s[72:73]
	s_waitcnt lgkmcnt(4)
	v_mfma_f32_16x16x32_f16 v[26:29], v[114:117], v[86:89], v[26:29]
	s_mov_b32 m0, s83
	v_mfma_f32_16x16x32_f16 v[30:33], v[118:121], v[86:89], v[30:33]
	global_load_lds_dwordx4 v169, s[72:73]
	s_waitcnt lgkmcnt(2)
	v_mfma_f32_16x16x32_f16 v[42:45], v[114:117], v[152:155], v[42:45]
	s_mov_b32 m0, s84
	v_mfma_f32_16x16x32_f16 v[46:49], v[118:121], v[152:155], v[46:49]
	global_load_lds_dwordx4 v170, s[72:73]
	v_mfma_f32_16x16x32_f16 v[34:37], v[114:117], v[148:151], v[34:37]
	s_mov_b32 m0, s85
	v_mfma_f32_16x16x32_f16 v[38:41], v[118:121], v[148:151], v[38:41]
	global_load_lds_dwordx4 v171, s[72:73]
	ds_read_b128 v[148:151], v125 offset:12288
	ds_read_b128 v[152:155], v125 offset:14336
	s_waitcnt lgkmcnt(3)
	ds_read_b128 v[176:179], v125 offset:16384
	ds_read_b128 v[180:183], v125 offset:18432
	v_mfma_f32_16x16x32_f16 v[82:85], v[114:117], v[156:159], v[50:53]
	s_mov_b32 m0, s86
	v_mfma_f32_16x16x32_f16 v[86:89], v[118:121], v[156:159], v[54:57]
	global_load_lds_dwordx4 v172, s[74:75]
	s_nop 1
	s_waitcnt lgkmcnt(4)
	v_mfma_f32_16x16x32_f16 v[90:93], v[114:117], v[160:163], v[58:61]
	s_mov_b32 m0, s87
	v_mfma_f32_16x16x32_f16 v[94:97], v[118:121], v[160:163], v[62:65]
	global_load_lds_dwordx4 v173, s[74:75]
	s_waitcnt lgkmcnt(3)
	v_mfma_f32_16x16x32_f16 v[98:101], v[114:117], v[148:151], v[66:69]
	v_mfma_f32_16x16x32_f16 v[102:105], v[118:121], v[148:151], v[70:73]
	s_waitcnt lgkmcnt(2)
	v_mfma_f32_16x16x32_f16 v[106:109], v[114:117], v[152:155], v[74:77]
	v_mfma_f32_16x16x32_f16 v[110:113], v[118:121], v[152:155], v[78:81]
	s_cbranch_vccnz .LBB3_132
	s_waitcnt lgkmcnt(1)
	v_mfma_f32_16x16x32_f16 v[10:13], v[114:117], v[176:179], v[10:13]
	v_mfma_f32_16x16x32_f16 v[14:17], v[118:121], v[176:179], v[14:17]
.LBB3_132:
	s_and_b64 vcc, exec, s[6:7]
	s_cbranch_vccnz .LBB3_134
	s_waitcnt lgkmcnt(0)
	v_mfma_f32_16x16x32_f16 v[2:5], v[114:117], v[180:183], v[2:5]
	v_mfma_f32_16x16x32_f16 v[6:9], v[118:121], v[180:183], v[6:9]

.LBB3_139:
	s_barrier
	s_waitcnt lgkmcnt(0)
	ds_read_b128 v[82:85], v122 offset:20480
	ds_read_b128 v[86:89], v122 offset:22528
	ds_read_b128 v[90:93], v136
	s_and_b64 vcc, exec, s[4:5]
	s_waitcnt lgkmcnt(0)
	v_mfma_f32_16x16x32_f16 v[50:53], v[82:85], v[90:93], v[50:53]
	v_mfma_f32_16x16x32_f16 v[54:57], v[86:89], v[90:93], v[54:57]
	ds_read_b128 v[90:93], v136 offset:2048
	ds_read_b128 v[148:151], v136 offset:4096
	ds_read_b128 v[152:155], v136 offset:6144
	ds_read_b128 v[156:159], v136 offset:8192
	ds_read_b128 v[160:163], v136 offset:10240
	s_waitcnt lgkmcnt(4)
	v_mfma_f32_16x16x32_f16 v[18:21], v[82:85], v[90:93], v[18:21]
	v_mfma_f32_16x16x32_f16 v[22:25], v[86:89], v[90:93], v[22:25]
	s_waitcnt lgkmcnt(3)
	v_mfma_f32_16x16x32_f16 v[58:61], v[82:85], v[148:151], v[58:61]
	v_mfma_f32_16x16x32_f16 v[62:65], v[86:89], v[148:151], v[62:65]
	ds_read_b128 v[148:151], v136 offset:12288
	s_waitcnt lgkmcnt(3)
	v_mfma_f32_16x16x32_f16 v[26:29], v[82:85], v[152:155], v[26:29]
	v_mfma_f32_16x16x32_f16 v[30:33], v[86:89], v[152:155], v[30:33]
	ds_read_b128 v[152:155], v136 offset:14336
	s_waitcnt lgkmcnt(3)
	ds_read_b128 v[176:179], v136 offset:16384
	ds_read_b128 v[180:183], v136 offset:18432
	v_mfma_f32_16x16x32_f16 v[66:69], v[82:85], v[156:159], v[66:69]
	v_mfma_f32_16x16x32_f16 v[70:73], v[86:89], v[156:159], v[70:73]
	s_waitcnt lgkmcnt(4)
	v_mfma_f32_16x16x32_f16 v[34:37], v[82:85], v[160:163], v[34:37]
	v_mfma_f32_16x16x32_f16 v[38:41], v[86:89], v[160:163], v[38:41]
	s_waitcnt lgkmcnt(3)
	v_mfma_f32_16x16x32_f16 v[74:77], v[82:85], v[148:151], v[74:77]
	v_mfma_f32_16x16x32_f16 v[78:81], v[86:89], v[148:151], v[78:81]
	s_waitcnt lgkmcnt(2)
	v_mfma_f32_16x16x32_f16 v[42:45], v[82:85], v[152:155], v[42:45]
	v_mfma_f32_16x16x32_f16 v[46:49], v[86:89], v[152:155], v[46:49]
	s_cbranch_vccnz .LBB3_141
	s_waitcnt lgkmcnt(1)
	v_mfma_f32_16x16x32_f16 v[10:13], v[82:85], v[176:179], v[10:13]
	v_mfma_f32_16x16x32_f16 v[14:17], v[86:89], v[176:179], v[14:17]

.LBB3_143:
	s_waitcnt lgkmcnt(0)
	ds_read_b128 v[82:85], v123 offset:20480
	ds_read_b128 v[86:89], v123 offset:22528
	ds_read_b128 v[90:93], v137
	ds_read_b128 v[94:97], v137 offset:2048
	ds_read_b128 v[148:151], v137 offset:4096
	ds_read_b128 v[152:155], v137 offset:6144
	ds_read_b128 v[156:159], v137 offset:8192
	ds_read_b128 v[160:163], v137 offset:10240
	s_and_b64 vcc, exec, s[4:5]
	s_waitcnt lgkmcnt(5)
	v_mfma_f32_16x16x32_f16 v[50:53], v[82:85], v[90:93], v[50:53]
	v_mfma_f32_16x16x32_f16 v[54:57], v[86:89], v[90:93], v[54:57]
	s_waitcnt lgkmcnt(4)
	v_mfma_f32_16x16x32_f16 v[18:21], v[82:85], v[94:97], v[18:21]
	v_mfma_f32_16x16x32_f16 v[22:25], v[86:89], v[94:97], v[22:25]
	s_waitcnt lgkmcnt(3)
	v_mfma_f32_16x16x32_f16 v[58:61], v[82:85], v[148:151], v[58:61]
	v_mfma_f32_16x16x32_f16 v[62:65], v[86:89], v[148:151], v[62:65]
	ds_read_b128 v[148:151], v137 offset:12288
	s_waitcnt lgkmcnt(3)
	v_mfma_f32_16x16x32_f16 v[26:29], v[82:85], v[152:155], v[26:29]
	v_mfma_f32_16x16x32_f16 v[30:33], v[86:89], v[152:155], v[30:33]
	ds_read_b128 v[152:155], v137 offset:14336
	s_waitcnt lgkmcnt(3)
	ds_read_b128 v[176:179], v137 offset:16384
	ds_read_b128 v[180:183], v137 offset:18432
	v_mfma_f32_16x16x32_f16 v[66:69], v[82:85], v[156:159], v[66:69]
	v_mfma_f32_16x16x32_f16 v[70:73], v[86:89], v[156:159], v[70:73]
	s_waitcnt lgkmcnt(4)
	v_mfma_f32_16x16x32_f16 v[34:37], v[82:85], v[160:163], v[34:37]
	v_mfma_f32_16x16x32_f16 v[38:41], v[86:89], v[160:163], v[38:41]
	s_waitcnt lgkmcnt(3)
	v_mfma_f32_16x16x32_f16 v[74:77], v[82:85], v[148:151], v[74:77]
	v_mfma_f32_16x16x32_f16 v[78:81], v[86:89], v[148:151], v[78:81]
	s_waitcnt lgkmcnt(2)
	v_mfma_f32_16x16x32_f16 v[42:45], v[82:85], v[152:155], v[42:45]
	v_mfma_f32_16x16x32_f16 v[46:49], v[86:89], v[152:155], v[46:49]
	s_cbranch_vccnz .LBB3_145
	s_waitcnt lgkmcnt(1)
	v_mfma_f32_16x16x32_f16 v[10:13], v[82:85], v[176:179], v[10:13]
	v_mfma_f32_16x16x32_f16 v[14:17], v[86:89], v[176:179], v[14:17]

.LBB3_147:
	s_waitcnt vmcnt(0)
	s_barrier
	s_waitcnt lgkmcnt(0)
	ds_read_b128 v[118:121], v124 offset:53248
	ds_read_b128 v[122:125], v124 offset:55296
	ds_read_b128 v[82:85], v136 offset:53248
	s_and_b64 vcc, exec, s[4:5]
	s_waitcnt lgkmcnt(0)
	v_mfma_f32_16x16x32_f16 v[50:53], v[118:121], v[82:85], v[50:53]
	v_mfma_f32_16x16x32_f16 v[54:57], v[122:125], v[82:85], v[54:57]
	ds_read_b128 v[82:85], v136 offset:55296
	ds_read_b128 v[148:151], v136 offset:57344
	ds_read_b128 v[152:155], v136 offset:59392
	ds_read_b128 v[156:159], v136 offset:63488
	ds_read_b128 v[160:163], v136 offset:61440
	s_waitcnt lgkmcnt(4)
	v_mfma_f32_16x16x32_f16 v[98:101], v[122:125], v[82:85], v[22:25]
	s_nop 2
	v_mfma_f32_16x16x32_f16 v[94:97], v[118:121], v[82:85], v[18:21]
	s_waitcnt lgkmcnt(3)
	v_mfma_f32_16x16x32_f16 v[18:21], v[118:121], v[148:151], v[58:61]
	s_nop 2
	s_waitcnt lgkmcnt(2)
	v_mfma_f32_16x16x32_f16 v[102:105], v[118:121], v[152:155], v[26:29]
	v_mfma_f32_16x16x32_f16 v[106:109], v[122:125], v[152:155], v[30:33]
	ds_read_b128 v[152:155], v138 offset:12288
	s_nop 1
	s_waitcnt lgkmcnt(2)
	v_mfma_f32_16x16x32_f16 v[110:113], v[122:125], v[156:159], v[38:41]
	s_nop 2
	s_waitcnt lgkmcnt(0)
	ds_read_b128 v[176:179], v138 offset:16384
	ds_read_b128 v[180:183], v138 offset:18432
	v_mfma_f32_16x16x32_f16 v[82:85], v[118:121], v[152:155], v[74:77]
	v_mfma_f32_16x16x32_f16 v[86:89], v[122:125], v[152:155], v[78:81]
	ds_read_b128 v[152:155], v138 offset:14336
	v_mfma_f32_16x16x32_f16 v[22:25], v[122:125], v[148:151], v[62:65]
	v_mfma_f32_16x16x32_f16 v[26:29], v[118:121], v[160:163], v[66:69]
	v_mfma_f32_16x16x32_f16 v[30:33], v[122:125], v[160:163], v[70:73]
	v_mfma_f32_16x16x32_f16 v[34:37], v[118:121], v[156:159], v[34:37]
	s_waitcnt lgkmcnt(0)
	v_mfma_f32_16x16x32_f16 v[114:117], v[118:121], v[152:155], v[42:45]
	v_mfma_f32_16x16x32_f16 v[90:93], v[122:125], v[152:155], v[46:49]
	s_cbranch_vccnz .LBB3_149
	s_waitcnt lgkmcnt(1)
	v_mfma_f32_16x16x32_f16 v[10:13], v[118:121], v[176:179], v[10:13]
	v_mfma_f32_16x16x32_f16 v[14:17], v[122:125], v[176:179], v[14:17]
.LBB3_149:
	s_and_b64 vcc, exec, s[6:7]
	s_cbranch_vccnz .LBB3_151
	s_waitcnt lgkmcnt(0)
	v_mfma_f32_16x16x32_f16 v[2:5], v[118:121], v[180:183], v[2:5]
	v_mfma_f32_16x16x32_f16 v[6:9], v[122:125], v[180:183], v[6:9]
.LBB3_151:
	ds_read_b128 v[118:121], v140 offset:53248
	ds_read_b128 v[122:125], v140 offset:55296
	ds_read_b128 v[38:41], v137 offset:53248
	ds_read_b128 v[42:45], v137 offset:55296
	s_load_dwordx2 s[0:1], s[0:1], 0x10
	s_and_b64 vcc, exec, s[4:5]
	s_waitcnt lgkmcnt(0)
	v_mfma_f32_16x16x32_f16 v[78:81], v[118:121], v[38:41], v[50:53]
	v_mfma_f32_16x16x32_f16 v[74:77], v[122:125], v[38:41], v[54:57]
	v_mfma_f32_16x16x32_f16 v[70:73], v[118:121], v[42:45], v[94:97]
	v_mfma_f32_16x16x32_f16 v[66:69], v[122:125], v[42:45], v[98:101]
	ds_read_b128 v[38:41], v137 offset:57344
	ds_read_b128 v[42:45], v137 offset:59392
	s_waitcnt lgkmcnt(0)
	v_mfma_f32_16x16x32_f16 v[62:65], v[118:121], v[38:41], v[18:21]
	v_mfma_f32_16x16x32_f16 v[58:61], v[122:125], v[38:41], v[22:25]
	s_nop 1
	ds_read_b128 v[18:21], v137 offset:61440
	ds_read_b128 v[22:25], v137 offset:63488
	v_mfma_f32_16x16x32_f16 v[54:57], v[118:121], v[42:45], v[102:105]
	v_mfma_f32_16x16x32_f16 v[50:53], v[122:125], v[42:45], v[106:109]
	s_waitcnt lgkmcnt(0)
	ds_read_b128 v[176:179], v139 offset:16384
	ds_read_b128 v[180:183], v139 offset:18432
	v_mfma_f32_16x16x32_f16 v[46:49], v[118:121], v[18:21], v[26:29]
	v_mfma_f32_16x16x32_f16 v[42:45], v[122:125], v[18:21], v[30:33]
	v_mfma_f32_16x16x32_f16 v[38:41], v[118:121], v[22:25], v[34:37]
	v_mfma_f32_16x16x32_f16 v[34:37], v[122:125], v[22:25], v[110:113]
	ds_read_b128 v[18:21], v139 offset:12288
	ds_read_b128 v[22:25], v139 offset:14336
	s_waitcnt lgkmcnt(0)
	v_mfma_f32_16x16x32_f16 v[30:33], v[118:121], v[18:21], v[82:85]
	v_mfma_f32_16x16x32_f16 v[26:29], v[122:125], v[18:21], v[86:89]
	v_mfma_f32_16x16x32_f16 v[18:21], v[118:121], v[22:25], v[114:117]
	v_mfma_f32_16x16x32_f16 v[22:25], v[122:125], v[22:25], v[90:93]
	s_cbranch_vccnz .LBB3_153
	s_waitcnt lgkmcnt(1)
	v_mfma_f32_16x16x32_f16 v[10:13], v[118:121], v[176:179], v[10:13]
	v_mfma_f32_16x16x32_f16 v[14:17], v[122:125], v[176:179], v[14:17]

	.amdhsa_kernel _Z8moe_gemmILi1EEvPKDF16_S1_PvPKyPKiPKfS1_
		.amdhsa_group_segment_fixed_size 0
		.amdhsa_private_segment_fixed_size 0
		.amdhsa_kernarg_size 56
		.amdhsa_user_sgpr_count 2
		.amdhsa_user_sgpr_dispatch_ptr 0
		.amdhsa_user_sgpr_queue_ptr 0
		.amdhsa_user_sgpr_kernarg_segment_ptr 1
		.amdhsa_user_sgpr_dispatch_id 0
		.amdhsa_user_sgpr_kernarg_preload_length 0
		.amdhsa_user_sgpr_kernarg_preload_offset 0
		.amdhsa_user_sgpr_private_segment_size 0
		.amdhsa_uses_dynamic_stack 0
		.amdhsa_enable_private_segment 0
		.amdhsa_system_sgpr_workgroup_id_x 1
		.amdhsa_system_sgpr_workgroup_id_y 0
		.amdhsa_system_sgpr_workgroup_id_z 0
		.amdhsa_system_sgpr_workgroup_info 0
		.amdhsa_system_vgpr_workitem_id 0
		.amdhsa_next_free_vgpr 184
		.amdhsa_next_free_sgpr 94
		.amdhsa_accum_offset 184
		.amdhsa_reserve_vcc 1
		.amdhsa_float_round_mode_32 0
		.amdhsa_float_round_mode_16_64 0
		.amdhsa_float_denorm_mode_32 3
		.amdhsa_float_denorm_mode_16_64 3
		.amdhsa_dx10_clamp 1
		.amdhsa_ieee_mode 1
		.amdhsa_fp16_overflow 0
		.amdhsa_tg_split 0
		.amdhsa_exception_fp_ieee_invalid_op 0
		.amdhsa_exception_fp_denorm_src 0
		.amdhsa_exception_fp_ieee_div_zero 0
		.amdhsa_exception_fp_ieee_overflow 0
		.amdhsa_exception_fp_ieee_underflow 0
		.amdhsa_exception_fp_ieee_inexact 0
		.amdhsa_exception_int_div_zero 0
	.end_amdhsa_kernel

.LBB4_98:
	v_add_u32_e32 v82, s36, v140
	v_add_u32_e32 v107, 0x5000, v82
	v_or_b32_e32 v106, v107, v141
	v_add_u32_e32 v142, 0, v106
	ds_read_b128 v[98:101], v142 offset:53248
	ds_read_b128 v[102:105], v142 offset:55296
	ds_read_b128 v[82:85], v137 offset:53248
	ds_read_b128 v[86:89], v137 offset:55296
	v_add_u32_e32 v140, 0xd000, v137
	s_and_b64 vcc, exec, s[24:25]
	s_waitcnt lgkmcnt(0)
	v_mfma_f32_16x16x32_f16 v[34:37], v[98:101], v[82:85], v[34:37]
	s_mov_b32 m0, s76
	v_mfma_f32_16x16x32_f16 v[38:41], v[102:105], v[82:85], v[38:41]
	global_load_lds_dwordx4 v176, s[72:73]
	v_mfma_f32_16x16x32_f16 v[42:45], v[98:101], v[86:89], v[42:45]
	s_mov_b32 m0, s77
	v_mfma_f32_16x16x32_f16 v[46:49], v[102:105], v[86:89], v[46:49]
	global_load_lds_dwordx4 v177, s[72:73]
	ds_read_b128 v[82:85], v137 offset:57344
	ds_read_b128 v[86:89], v137 offset:59392
	s_waitcnt lgkmcnt(0)
	v_mfma_f32_16x16x32_f16 v[50:53], v[98:101], v[82:85], v[50:53]
	s_mov_b32 m0, s78
	v_mfma_f32_16x16x32_f16 v[54:57], v[102:105], v[82:85], v[54:57]
	global_load_lds_dwordx4 v178, s[72:73]
	v_mfma_f32_16x16x32_f16 v[58:61], v[98:101], v[86:89], v[58:61]
	s_mov_b32 m0, s79
	v_mfma_f32_16x16x32_f16 v[62:65], v[102:105], v[86:89], v[62:65]
	global_load_lds_dwordx4 v179, s[72:73]
	ds_read_b128 v[82:85], v137 offset:61440
	ds_read_b128 v[86:89], v137 offset:63488
	s_waitcnt lgkmcnt(0)
	ds_read_b128 v[184:187], v140 offset:16384
	ds_read_b128 v[188:191], v140 offset:18432
	v_mfma_f32_16x16x32_f16 v[66:69], v[98:101], v[82:85], v[66:69]
	s_mov_b32 m0, s80
	v_mfma_f32_16x16x32_f16 v[70:73], v[102:105], v[82:85], v[70:73]
	global_load_lds_dwordx4 v180, s[74:75]
	v_mfma_f32_16x16x32_f16 v[82:85], v[102:105], v[86:89], v[18:21]
	s_nop 2
	ds_read_b128 v[18:21], v140 offset:12288
	ds_read_b128 v[148:151], v140 offset:14336
	s_mov_b32 m0, s81
	v_mfma_f32_16x16x32_f16 v[74:77], v[98:101], v[86:89], v[74:77]
	global_load_lds_dwordx4 v181, s[74:75]
	s_waitcnt lgkmcnt(0)
	v_mfma_f32_16x16x32_f16 v[86:89], v[98:101], v[18:21], v[22:25]
	v_mfma_f32_16x16x32_f16 v[90:93], v[102:105], v[18:21], v[26:29]
	v_mfma_f32_16x16x32_f16 v[94:97], v[98:101], v[148:151], v[30:33]
	v_mfma_f32_16x16x32_f16 v[78:81], v[102:105], v[148:151], v[78:81]
	s_cbranch_vccnz .LBB4_100
	s_waitcnt lgkmcnt(1)
	v_mfma_f32_16x16x32_f16 v[6:9], v[98:101], v[184:187], v[6:9]
	v_mfma_f32_16x16x32_f16 v[2:5], v[102:105], v[184:187], v[2:5]
.LBB4_100:
	s_and_b64 vcc, exec, s[26:27]
	s_cbranch_vccnz .LBB4_102
	s_waitcnt lgkmcnt(0)
	v_mfma_f32_16x16x32_f16 v[10:13], v[98:101], v[188:191], v[10:13]
	v_mfma_f32_16x16x32_f16 v[14:17], v[102:105], v[188:191], v[14:17]

.LBB4_109:
	s_and_b64 vcc, exec, s[24:25]
	s_waitcnt lgkmcnt(5)
	v_mfma_f32_16x16x32_f16 v[22:25], v[86:89], v[92:95], v[22:25]
	s_mov_b32 m0, s82
	v_mfma_f32_16x16x32_f16 v[18:21], v[82:85], v[92:95], v[18:21]
	global_load_lds_dwordx4 v176, s[72:73]
	s_waitcnt lgkmcnt(4)
	v_mfma_f32_16x16x32_f16 v[26:29], v[82:85], v[96:99], v[26:29]
	s_mov_b32 m0, s83
	v_mfma_f32_16x16x32_f16 v[30:33], v[86:89], v[96:99], v[30:33]
	global_load_lds_dwordx4 v177, s[72:73]
	s_waitcnt lgkmcnt(3)
	v_mfma_f32_16x16x32_f16 v[34:37], v[82:85], v[156:159], v[34:37]
	s_mov_b32 m0, s84
	v_mfma_f32_16x16x32_f16 v[38:41], v[86:89], v[156:159], v[38:41]
	global_load_lds_dwordx4 v178, s[72:73]
	ds_read_b128 v[156:159], v146 offset:12288
	s_waitcnt lgkmcnt(3)
	v_mfma_f32_16x16x32_f16 v[42:45], v[82:85], v[160:163], v[42:45]
	s_mov_b32 m0, s85
	v_mfma_f32_16x16x32_f16 v[46:49], v[86:89], v[160:163], v[46:49]
	global_load_lds_dwordx4 v179, s[72:73]
	ds_read_b128 v[160:163], v146 offset:14336
	s_waitcnt lgkmcnt(3)
	ds_read_b128 v[184:187], v146 offset:16384
	ds_read_b128 v[188:191], v146 offset:18432
	v_mfma_f32_16x16x32_f16 v[50:53], v[82:85], v[164:167], v[50:53]
	s_mov_b32 m0, s86
	v_mfma_f32_16x16x32_f16 v[54:57], v[86:89], v[164:167], v[54:57]
	global_load_lds_dwordx4 v180, s[74:75]
	s_waitcnt lgkmcnt(4)
	v_mfma_f32_16x16x32_f16 v[58:61], v[82:85], v[168:171], v[58:61]
	s_mov_b32 m0, s87
	v_mfma_f32_16x16x32_f16 v[62:65], v[86:89], v[168:171], v[62:65]
	global_load_lds_dwordx4 v181, s[74:75]
	s_waitcnt lgkmcnt(3)
	v_mfma_f32_16x16x32_f16 v[66:69], v[82:85], v[156:159], v[66:69]
	v_mfma_f32_16x16x32_f16 v[70:73], v[86:89], v[156:159], v[70:73]
	s_waitcnt lgkmcnt(2)
	v_mfma_f32_16x16x32_f16 v[74:77], v[82:85], v[160:163], v[74:77]
	v_mfma_f32_16x16x32_f16 v[78:81], v[86:89], v[160:163], v[78:81]
	s_cbranch_vccnz .LBB4_111
	s_waitcnt lgkmcnt(1)
	v_mfma_f32_16x16x32_f16 v[6:9], v[82:85], v[184:187], v[6:9]
	v_mfma_f32_16x16x32_f16 v[2:5], v[86:89], v[184:187], v[2:5]
.LBB4_111:
	s_and_b64 vcc, exec, s[26:27]
	s_cbranch_vccnz .LBB4_113
	s_waitcnt lgkmcnt(0)
	v_mfma_f32_16x16x32_f16 v[10:13], v[82:85], v[188:191], v[10:13]
	v_mfma_f32_16x16x32_f16 v[14:17], v[86:89], v[188:191], v[14:17]
.LBB4_113:
	s_waitcnt lgkmcnt(0)
	v_add_u32_e32 v148, s35, v107
	ds_read_b128 v[82:85], v148
	ds_read_b128 v[86:89], v148 offset:2048
	v_add_u32_e32 v147, s35, v147
	ds_read_b128 v[92:95], v147
	ds_read_b128 v[96:99], v147 offset:2048
	ds_read_b128 v[156:159], v147 offset:4096
	ds_read_b128 v[160:163], v147 offset:6144
	ds_read_b128 v[164:167], v147 offset:8192
	ds_read_b128 v[168:171], v147 offset:10240
	s_and_b64 vcc, exec, s[24:25]
	s_waitcnt lgkmcnt(5)
	v_mfma_f32_16x16x32_f16 v[22:25], v[86:89], v[92:95], v[22:25]
	v_mfma_f32_16x16x32_f16 v[18:21], v[82:85], v[92:95], v[18:21]
	s_waitcnt lgkmcnt(4)
	v_mfma_f32_16x16x32_f16 v[26:29], v[82:85], v[96:99], v[26:29]
	v_mfma_f32_16x16x32_f16 v[30:33], v[86:89], v[96:99], v[30:33]
	s_waitcnt lgkmcnt(3)
	v_mfma_f32_16x16x32_f16 v[34:37], v[82:85], v[156:159], v[34:37]
	v_mfma_f32_16x16x32_f16 v[38:41], v[86:89], v[156:159], v[38:41]
	ds_read_b128 v[156:159], v147 offset:12288
	s_waitcnt lgkmcnt(3)
	v_mfma_f32_16x16x32_f16 v[42:45], v[82:85], v[160:163], v[42:45]
	v_mfma_f32_16x16x32_f16 v[46:49], v[86:89], v[160:163], v[46:49]
	ds_read_b128 v[160:163], v147 offset:14336
	s_waitcnt lgkmcnt(3)
	ds_read_b128 v[184:187], v147 offset:16384
	ds_read_b128 v[188:191], v147 offset:18432
	v_mfma_f32_16x16x32_f16 v[50:53], v[82:85], v[164:167], v[50:53]
	v_mfma_f32_16x16x32_f16 v[54:57], v[86:89], v[164:167], v[54:57]
	s_waitcnt lgkmcnt(4)
	v_mfma_f32_16x16x32_f16 v[58:61], v[82:85], v[168:171], v[58:61]
	v_mfma_f32_16x16x32_f16 v[62:65], v[86:89], v[168:171], v[62:65]
	s_waitcnt lgkmcnt(3)
	v_mfma_f32_16x16x32_f16 v[66:69], v[82:85], v[156:159], v[66:69]
	v_mfma_f32_16x16x32_f16 v[70:73], v[86:89], v[156:159], v[70:73]
	s_waitcnt lgkmcnt(2)
	v_mfma_f32_16x16x32_f16 v[74:77], v[82:85], v[160:163], v[74:77]
	v_mfma_f32_16x16x32_f16 v[78:81], v[86:89], v[160:163], v[78:81]
	s_cbranch_vccnz .LBB4_115
	s_waitcnt lgkmcnt(1)
	v_mfma_f32_16x16x32_f16 v[6:9], v[82:85], v[184:187], v[6:9]
	v_mfma_f32_16x16x32_f16 v[2:5], v[86:89], v[184:187], v[2:5]

.LBB4_123:
	s_and_b64 vcc, exec, s[24:25]
	s_waitcnt lgkmcnt(5)
	v_mfma_f32_16x16x32_f16 v[18:21], v[82:85], v[92:95], v[18:21]
	s_mov_b32 m0, s88
	v_mfma_f32_16x16x32_f16 v[22:25], v[86:89], v[92:95], v[22:25]
	global_load_lds_dwordx4 v176, s[72:73]
	s_waitcnt lgkmcnt(4)
	v_mfma_f32_16x16x32_f16 v[26:29], v[82:85], v[96:99], v[26:29]
	s_mov_b32 m0, s89
	v_mfma_f32_16x16x32_f16 v[30:33], v[86:89], v[96:99], v[30:33]
	global_load_lds_dwordx4 v177, s[72:73]
	s_waitcnt lgkmcnt(3)
	v_mfma_f32_16x16x32_f16 v[34:37], v[82:85], v[156:159], v[34:37]
	s_mov_b32 m0, s90
	v_mfma_f32_16x16x32_f16 v[38:41], v[86:89], v[156:159], v[38:41]
	global_load_lds_dwordx4 v178, s[72:73]
	ds_read_b128 v[156:159], v137 offset:12288
	s_waitcnt lgkmcnt(3)
	v_mfma_f32_16x16x32_f16 v[42:45], v[82:85], v[160:163], v[42:45]
	s_mov_b32 m0, s91
	v_mfma_f32_16x16x32_f16 v[46:49], v[86:89], v[160:163], v[46:49]
	global_load_lds_dwordx4 v179, s[72:73]
	ds_read_b128 v[160:163], v137 offset:14336
	s_waitcnt lgkmcnt(3)
	ds_read_b128 v[184:187], v137 offset:16384
	ds_read_b128 v[188:191], v137 offset:18432
	v_mfma_f32_16x16x32_f16 v[50:53], v[82:85], v[164:167], v[50:53]
	s_mov_b32 m0, s92
	v_mfma_f32_16x16x32_f16 v[54:57], v[86:89], v[164:167], v[54:57]
	global_load_lds_dwordx4 v180, s[74:75]
	s_waitcnt lgkmcnt(4)
	v_mfma_f32_16x16x32_f16 v[58:61], v[82:85], v[168:171], v[58:61]
	s_mov_b32 m0, s93
	v_mfma_f32_16x16x32_f16 v[62:65], v[86:89], v[168:171], v[62:65]
	global_load_lds_dwordx4 v181, s[74:75]
	s_waitcnt lgkmcnt(3)
	v_mfma_f32_16x16x32_f16 v[66:69], v[82:85], v[156:159], v[66:69]
	v_mfma_f32_16x16x32_f16 v[70:73], v[86:89], v[156:159], v[70:73]
	s_waitcnt lgkmcnt(2)
	v_mfma_f32_16x16x32_f16 v[74:77], v[82:85], v[160:163], v[74:77]
	v_mfma_f32_16x16x32_f16 v[78:81], v[86:89], v[160:163], v[78:81]
	s_cbranch_vccnz .LBB4_125
	s_waitcnt lgkmcnt(1)
	v_mfma_f32_16x16x32_f16 v[6:9], v[82:85], v[184:187], v[6:9]
	v_mfma_f32_16x16x32_f16 v[2:5], v[86:89], v[184:187], v[2:5]

.LBB4_134:
	s_and_b64 vcc, exec, s[24:25]
	s_waitcnt lgkmcnt(5)
	v_mfma_f32_16x16x32_f16 v[18:21], v[82:85], v[92:95], v[18:21]
	s_mov_b32 m0, s76
	v_mfma_f32_16x16x32_f16 v[22:25], v[86:89], v[92:95], v[22:25]
	global_load_lds_dwordx4 v176, s[72:73]
	s_waitcnt lgkmcnt(4)
	v_mfma_f32_16x16x32_f16 v[26:29], v[82:85], v[96:99], v[26:29]
	s_mov_b32 m0, s77
	v_mfma_f32_16x16x32_f16 v[30:33], v[86:89], v[96:99], v[30:33]
	global_load_lds_dwordx4 v177, s[72:73]
	s_waitcnt lgkmcnt(3)
	v_mfma_f32_16x16x32_f16 v[34:37], v[82:85], v[156:159], v[34:37]
	s_mov_b32 m0, s78
	v_mfma_f32_16x16x32_f16 v[38:41], v[86:89], v[156:159], v[38:41]
	global_load_lds_dwordx4 v178, s[72:73]
	ds_read_b128 v[156:159], v140 offset:12288
	s_waitcnt lgkmcnt(3)
	v_mfma_f32_16x16x32_f16 v[42:45], v[82:85], v[160:163], v[42:45]
	s_mov_b32 m0, s79
	v_mfma_f32_16x16x32_f16 v[46:49], v[86:89], v[160:163], v[46:49]
	global_load_lds_dwordx4 v179, s[72:73]
	ds_read_b128 v[160:163], v140 offset:14336
	s_waitcnt lgkmcnt(3)
	ds_read_b128 v[184:187], v140 offset:16384
	ds_read_b128 v[188:191], v140 offset:18432
	v_mfma_f32_16x16x32_f16 v[50:53], v[82:85], v[164:167], v[50:53]
	s_mov_b32 m0, s80
	v_mfma_f32_16x16x32_f16 v[54:57], v[86:89], v[164:167], v[54:57]
	global_load_lds_dwordx4 v180, s[74:75]
	s_waitcnt lgkmcnt(4)
	v_mfma_f32_16x16x32_f16 v[58:61], v[82:85], v[168:171], v[58:61]
	s_mov_b32 m0, s81
	v_mfma_f32_16x16x32_f16 v[62:65], v[86:89], v[168:171], v[62:65]
	global_load_lds_dwordx4 v181, s[74:75]
	s_waitcnt lgkmcnt(3)
	v_mfma_f32_16x16x32_f16 v[66:69], v[82:85], v[156:159], v[66:69]
	v_mfma_f32_16x16x32_f16 v[70:73], v[86:89], v[156:159], v[70:73]
	s_waitcnt lgkmcnt(2)
	v_mfma_f32_16x16x32_f16 v[74:77], v[82:85], v[160:163], v[74:77]
	v_mfma_f32_16x16x32_f16 v[78:81], v[86:89], v[160:163], v[78:81]
	s_cbranch_vccnz .LBB4_136
	s_waitcnt lgkmcnt(1)
	v_mfma_f32_16x16x32_f16 v[6:9], v[82:85], v[184:187], v[6:9]
	v_mfma_f32_16x16x32_f16 v[2:5], v[86:89], v[184:187], v[2:5]

.LBB4_145:
	s_waitcnt lgkmcnt(0)
	ds_read_b128 v[114:117], v90
	ds_read_b128 v[118:121], v90 offset:2048
	ds_read_b128 v[82:85], v146
	ds_read_b128 v[86:89], v146 offset:2048
	ds_read_b128 v[156:159], v146 offset:4096
	ds_read_b128 v[160:163], v146 offset:6144
	ds_read_b128 v[164:167], v146 offset:8192
	ds_read_b128 v[168:171], v146 offset:10240
	s_and_b64 vcc, exec, s[24:25]
	s_waitcnt lgkmcnt(5)
	v_mfma_f32_16x16x32_f16 v[18:21], v[114:117], v[82:85], v[18:21]
	s_mov_b32 m0, s82
	v_mfma_f32_16x16x32_f16 v[22:25], v[118:121], v[82:85], v[22:25]
	global_load_lds_dwordx4 v176, s[72:73]
	s_waitcnt lgkmcnt(4)
	v_mfma_f32_16x16x32_f16 v[26:29], v[114:117], v[86:89], v[26:29]
	s_mov_b32 m0, s83
	v_mfma_f32_16x16x32_f16 v[30:33], v[118:121], v[86:89], v[30:33]
	global_load_lds_dwordx4 v177, s[72:73]
	s_waitcnt lgkmcnt(2)
	v_mfma_f32_16x16x32_f16 v[42:45], v[114:117], v[160:163], v[42:45]
	s_mov_b32 m0, s84
	v_mfma_f32_16x16x32_f16 v[46:49], v[118:121], v[160:163], v[46:49]
	global_load_lds_dwordx4 v178, s[72:73]
	v_mfma_f32_16x16x32_f16 v[34:37], v[114:117], v[156:159], v[34:37]
	s_mov_b32 m0, s85
	v_mfma_f32_16x16x32_f16 v[38:41], v[118:121], v[156:159], v[38:41]
	global_load_lds_dwordx4 v179, s[72:73]
	ds_read_b128 v[156:159], v146 offset:12288
	ds_read_b128 v[160:163], v146 offset:14336
	s_waitcnt lgkmcnt(3)
	ds_read_b128 v[184:187], v146 offset:16384
	ds_read_b128 v[188:191], v146 offset:18432
	v_mfma_f32_16x16x32_f16 v[82:85], v[114:117], v[164:167], v[50:53]
	s_mov_b32 m0, s86
	v_mfma_f32_16x16x32_f16 v[86:89], v[118:121], v[164:167], v[54:57]
	global_load_lds_dwordx4 v180, s[74:75]
	s_nop 1
	s_waitcnt lgkmcnt(4)
	v_mfma_f32_16x16x32_f16 v[90:93], v[114:117], v[168:171], v[58:61]
	s_mov_b32 m0, s87
	v_mfma_f32_16x16x32_f16 v[94:97], v[118:121], v[168:171], v[62:65]
	global_load_lds_dwordx4 v181, s[74:75]
	s_waitcnt lgkmcnt(3)
	v_mfma_f32_16x16x32_f16 v[98:101], v[114:117], v[156:159], v[66:69]
	v_mfma_f32_16x16x32_f16 v[102:105], v[118:121], v[156:159], v[70:73]
	s_waitcnt lgkmcnt(2)
	v_mfma_f32_16x16x32_f16 v[106:109], v[114:117], v[160:163], v[74:77]
	v_mfma_f32_16x16x32_f16 v[110:113], v[118:121], v[160:163], v[78:81]
	s_cbranch_vccnz .LBB4_147
	s_waitcnt lgkmcnt(1)
	v_mfma_f32_16x16x32_f16 v[6:9], v[114:117], v[184:187], v[6:9]
	v_mfma_f32_16x16x32_f16 v[2:5], v[118:121], v[184:187], v[2:5]
.LBB4_147:
	s_and_b64 vcc, exec, s[26:27]
	s_cbranch_vccnz .LBB4_149
	s_waitcnt lgkmcnt(0)
	v_mfma_f32_16x16x32_f16 v[10:13], v[114:117], v[188:191], v[10:13]
	v_mfma_f32_16x16x32_f16 v[14:17], v[118:121], v[188:191], v[14:17]

.LBB4_154:
	s_barrier
	s_waitcnt lgkmcnt(0)
	ds_read_b128 v[82:85], v138 offset:20480
	ds_read_b128 v[86:89], v138 offset:22528
	ds_read_b128 v[90:93], v137
	s_and_b64 vcc, exec, s[24:25]
	s_waitcnt lgkmcnt(0)
	v_mfma_f32_16x16x32_f16 v[50:53], v[82:85], v[90:93], v[50:53]
	v_mfma_f32_16x16x32_f16 v[54:57], v[86:89], v[90:93], v[54:57]
	ds_read_b128 v[90:93], v137 offset:2048
	ds_read_b128 v[156:159], v137 offset:4096
	ds_read_b128 v[160:163], v137 offset:6144
	ds_read_b128 v[164:167], v137 offset:8192
	ds_read_b128 v[168:171], v137 offset:10240
	s_waitcnt lgkmcnt(4)
	v_mfma_f32_16x16x32_f16 v[18:21], v[82:85], v[90:93], v[18:21]
	v_mfma_f32_16x16x32_f16 v[22:25], v[86:89], v[90:93], v[22:25]
	s_waitcnt lgkmcnt(3)
	v_mfma_f32_16x16x32_f16 v[58:61], v[82:85], v[156:159], v[58:61]
	v_mfma_f32_16x16x32_f16 v[62:65], v[86:89], v[156:159], v[62:65]
	ds_read_b128 v[156:159], v137 offset:12288
	s_waitcnt lgkmcnt(3)
	v_mfma_f32_16x16x32_f16 v[26:29], v[82:85], v[160:163], v[26:29]
	v_mfma_f32_16x16x32_f16 v[30:33], v[86:89], v[160:163], v[30:33]
	ds_read_b128 v[160:163], v137 offset:14336
	s_waitcnt lgkmcnt(3)
	ds_read_b128 v[184:187], v137 offset:16384
	ds_read_b128 v[188:191], v137 offset:18432
	v_mfma_f32_16x16x32_f16 v[66:69], v[82:85], v[164:167], v[66:69]
	v_mfma_f32_16x16x32_f16 v[70:73], v[86:89], v[164:167], v[70:73]
	s_waitcnt lgkmcnt(4)
	v_mfma_f32_16x16x32_f16 v[34:37], v[82:85], v[168:171], v[34:37]
	v_mfma_f32_16x16x32_f16 v[38:41], v[86:89], v[168:171], v[38:41]
	s_waitcnt lgkmcnt(3)
	v_mfma_f32_16x16x32_f16 v[74:77], v[82:85], v[156:159], v[74:77]
	v_mfma_f32_16x16x32_f16 v[78:81], v[86:89], v[156:159], v[78:81]
	s_waitcnt lgkmcnt(2)
	v_mfma_f32_16x16x32_f16 v[42:45], v[82:85], v[160:163], v[42:45]
	v_mfma_f32_16x16x32_f16 v[46:49], v[86:89], v[160:163], v[46:49]
	s_cbranch_vccnz .LBB4_156
	s_waitcnt lgkmcnt(1)
	v_mfma_f32_16x16x32_f16 v[6:9], v[82:85], v[184:187], v[6:9]
	v_mfma_f32_16x16x32_f16 v[2:5], v[86:89], v[184:187], v[2:5]

.LBB4_158:
	s_waitcnt lgkmcnt(0)
	ds_read_b128 v[82:85], v139 offset:20480
	ds_read_b128 v[86:89], v139 offset:22528
	ds_read_b128 v[90:93], v0
	ds_read_b128 v[94:97], v0 offset:2048
	ds_read_b128 v[156:159], v0 offset:4096
	ds_read_b128 v[160:163], v0 offset:6144
	ds_read_b128 v[164:167], v0 offset:8192
	ds_read_b128 v[168:171], v0 offset:10240
	s_and_b64 vcc, exec, s[24:25]
	s_waitcnt lgkmcnt(5)
	v_mfma_f32_16x16x32_f16 v[50:53], v[82:85], v[90:93], v[50:53]
	v_mfma_f32_16x16x32_f16 v[54:57], v[86:89], v[90:93], v[54:57]
	s_waitcnt lgkmcnt(4)
	v_mfma_f32_16x16x32_f16 v[18:21], v[82:85], v[94:97], v[18:21]
	v_mfma_f32_16x16x32_f16 v[22:25], v[86:89], v[94:97], v[22:25]
	s_waitcnt lgkmcnt(3)
	v_mfma_f32_16x16x32_f16 v[58:61], v[82:85], v[156:159], v[58:61]
	v_mfma_f32_16x16x32_f16 v[62:65], v[86:89], v[156:159], v[62:65]
	ds_read_b128 v[156:159], v0 offset:12288
	s_waitcnt lgkmcnt(3)
	v_mfma_f32_16x16x32_f16 v[26:29], v[82:85], v[160:163], v[26:29]
	v_mfma_f32_16x16x32_f16 v[30:33], v[86:89], v[160:163], v[30:33]
	ds_read_b128 v[160:163], v0 offset:14336
	s_waitcnt lgkmcnt(3)
	ds_read_b128 v[184:187], v0 offset:16384
	ds_read_b128 v[188:191], v0 offset:18432
	v_mfma_f32_16x16x32_f16 v[66:69], v[82:85], v[164:167], v[66:69]
	v_mfma_f32_16x16x32_f16 v[70:73], v[86:89], v[164:167], v[70:73]
	s_waitcnt lgkmcnt(4)
	v_mfma_f32_16x16x32_f16 v[34:37], v[82:85], v[168:171], v[34:37]
	v_mfma_f32_16x16x32_f16 v[38:41], v[86:89], v[168:171], v[38:41]
	s_waitcnt lgkmcnt(3)
	v_mfma_f32_16x16x32_f16 v[74:77], v[82:85], v[156:159], v[74:77]
	v_mfma_f32_16x16x32_f16 v[78:81], v[86:89], v[156:159], v[78:81]
	s_waitcnt lgkmcnt(2)
	v_mfma_f32_16x16x32_f16 v[42:45], v[82:85], v[160:163], v[42:45]
	v_mfma_f32_16x16x32_f16 v[46:49], v[86:89], v[160:163], v[46:49]
	s_cbranch_vccnz .LBB4_160
	s_waitcnt lgkmcnt(1)
	v_mfma_f32_16x16x32_f16 v[6:9], v[82:85], v[184:187], v[6:9]
	v_mfma_f32_16x16x32_f16 v[2:5], v[86:89], v[184:187], v[2:5]

.LBB4_166:
	ds_read_b128 v[114:117], v143 offset:53248
	ds_read_b128 v[118:121], v143 offset:55296
	ds_read_b128 v[42:45], v0 offset:53248
	ds_read_b128 v[46:49], v0 offset:55296
	s_load_dwordx2 s[0:1], s[0:1], 0x10
	s_and_b64 vcc, exec, s[24:25]
	s_waitcnt lgkmcnt(0)
	v_mfma_f32_16x16x32_f16 v[74:77], v[114:117], v[42:45], v[50:53]
	v_mfma_f32_16x16x32_f16 v[78:81], v[118:121], v[42:45], v[54:57]
	v_mfma_f32_16x16x32_f16 v[66:69], v[114:117], v[46:49], v[94:97]
	v_mfma_f32_16x16x32_f16 v[70:73], v[118:121], v[46:49], v[98:101]
	ds_read_b128 v[42:45], v0 offset:57344
	ds_read_b128 v[46:49], v0 offset:59392
	s_waitcnt lgkmcnt(0)
	v_mfma_f32_16x16x32_f16 v[58:61], v[114:117], v[42:45], v[18:21]
	v_mfma_f32_16x16x32_f16 v[62:65], v[118:121], v[42:45], v[22:25]
	s_nop 1
	ds_read_b128 v[18:21], v0 offset:61440
	ds_read_b128 v[22:25], v0 offset:63488
	v_mfma_f32_16x16x32_f16 v[50:53], v[114:117], v[46:49], v[102:105]
	v_mfma_f32_16x16x32_f16 v[54:57], v[118:121], v[46:49], v[106:109]
	s_waitcnt lgkmcnt(0)
	ds_read_b128 v[184:187], v141 offset:16384
	ds_read_b128 v[188:191], v141 offset:18432
	v_mfma_f32_16x16x32_f16 v[42:45], v[114:117], v[18:21], v[26:29]
	v_mfma_f32_16x16x32_f16 v[46:49], v[118:121], v[18:21], v[30:33]
	v_mfma_f32_16x16x32_f16 v[34:37], v[114:117], v[22:25], v[34:37]
	v_mfma_f32_16x16x32_f16 v[38:41], v[118:121], v[22:25], v[38:41]
	ds_read_b128 v[18:21], v141 offset:12288
	ds_read_b128 v[22:25], v141 offset:14336
	s_waitcnt lgkmcnt(0)
	v_mfma_f32_16x16x32_f16 v[26:29], v[114:117], v[18:21], v[82:85]
	v_mfma_f32_16x16x32_f16 v[30:33], v[118:121], v[18:21], v[86:89]
	v_mfma_f32_16x16x32_f16 v[18:21], v[114:117], v[22:25], v[110:113]
	v_mfma_f32_16x16x32_f16 v[22:25], v[118:121], v[22:25], v[90:93]
	s_cbranch_vccnz .LBB4_168
	s_waitcnt lgkmcnt(1)
	v_mfma_f32_16x16x32_f16 v[6:9], v[114:117], v[184:187], v[6:9]
	v_mfma_f32_16x16x32_f16 v[2:5], v[118:121], v[184:187], v[2:5]

	.amdhsa_kernel _Z8moe_gemmILi2EEvPKDF16_S1_PvPKyPKiPKfS1_
		.amdhsa_group_segment_fixed_size 0
		.amdhsa_private_segment_fixed_size 0
		.amdhsa_kernarg_size 56
		.amdhsa_user_sgpr_count 2
		.amdhsa_user_sgpr_dispatch_ptr 0
		.amdhsa_user_sgpr_queue_ptr 0
		.amdhsa_user_sgpr_kernarg_segment_ptr 1
		.amdhsa_user_sgpr_dispatch_id 0
		.amdhsa_user_sgpr_kernarg_preload_length 0
		.amdhsa_user_sgpr_kernarg_preload_offset 0
		.amdhsa_user_sgpr_private_segment_size 0
		.amdhsa_uses_dynamic_stack 0
		.amdhsa_enable_private_segment 0
		.amdhsa_system_sgpr_workgroup_id_x 1
		.amdhsa_system_sgpr_workgroup_id_y 0
		.amdhsa_system_sgpr_workgroup_id_z 0
		.amdhsa_system_sgpr_workgroup_info 0
		.amdhsa_system_vgpr_workitem_id 0
		.amdhsa_next_free_vgpr 192
		.amdhsa_next_free_sgpr 94
		.amdhsa_accum_offset 192
		.amdhsa_reserve_vcc 1
		.amdhsa_float_round_mode_32 0
		.amdhsa_float_round_mode_16_64 0
		.amdhsa_float_denorm_mode_32 3
		.amdhsa_float_denorm_mode_16_64 3
		.amdhsa_dx10_clamp 1
		.amdhsa_ieee_mode 1
		.amdhsa_fp16_overflow 0
		.amdhsa_tg_split 0
		.amdhsa_exception_fp_ieee_invalid_op 0
		.amdhsa_exception_fp_denorm_src 0
		.amdhsa_exception_fp_ieee_div_zero 0
		.amdhsa_exception_fp_ieee_overflow 0
		.amdhsa_exception_fp_ieee_underflow 0
		.amdhsa_exception_fp_ieee_inexact 0
		.amdhsa_exception_int_div_zero 0
	.end_amdhsa_kernel

amdhsa.kernels:
  - .agpr_count:     0
    .args:
      - .actual_access:  write_only
        .address_space:  global
        .offset:         0
        .size:           8
        .value_kind:     global_buffer
    .group_segment_fixed_size: 0
    .kernarg_segment_align: 8
    .kernarg_segment_size: 8
    .language:       OpenCL C
    .language_version:
      - 2
      - 0
    .max_flat_workgroup_size: 1024
    .name:           _Z15zero_cnt_kernelPy
    .private_segment_fixed_size: 0
    .sgpr_count:     10
    .sgpr_spill_count: 0
    .symbol:         _Z15zero_cnt_kernelPy.kd
    .uniform_work_group_size: 1
    .uses_dynamic_stack: false
    .vgpr_count:     3
    .vgpr_spill_count: 0
    .wavefront_size: 64
  - .agpr_count:     0
    .args:
      - .actual_access:  read_only
        .address_space:  global
        .offset:         0
        .size:           8
        .value_kind:     global_buffer
      - .actual_access:  read_only
        .address_space:  global
        .offset:         8
        .size:           8
        .value_kind:     global_buffer
      - .actual_access:  read_only
        .address_space:  global
        .offset:         16
        .size:           8
        .value_kind:     global_buffer
      - .actual_access:  read_only
        .address_space:  global
        .offset:         24
        .size:           8
        .value_kind:     global_buffer
      - .actual_access:  write_only
        .address_space:  global
        .offset:         32
        .size:           8
        .value_kind:     global_buffer
      - .actual_access:  write_only
        .address_space:  global
        .offset:         40
        .size:           8
        .value_kind:     global_buffer
      - .actual_access:  write_only
        .address_space:  global
        .offset:         48
        .size:           8
        .value_kind:     global_buffer
      - .address_space:  global
        .offset:         56
        .size:           8
        .value_kind:     global_buffer
      - .actual_access:  write_only
        .address_space:  global
        .offset:         64
        .size:           8
        .value_kind:     global_buffer
      - .actual_access:  write_only
        .address_space:  global
        .offset:         72
        .size:           8
        .value_kind:     global_buffer
    .group_segment_fixed_size: 0
    .kernarg_segment_align: 8
    .kernarg_segment_size: 80
    .language:       OpenCL C
    .language_version:
      - 2
      - 0
    .max_flat_workgroup_size: 256
    .name:           _Z11prep_kernelPKfS0_S0_S0_PDF16_S1_S1_PyPiPf
    .private_segment_fixed_size: 0
    .sgpr_count:     55
    .sgpr_spill_count: 0
    .symbol:         _Z11prep_kernelPKfS0_S0_S0_PDF16_S1_S1_PyPiPf.kd
    .uniform_work_group_size: 1
    .uses_dynamic_stack: false
    .vgpr_count:     248
    .vgpr_spill_count: 0
    .wavefront_size: 64
  - .agpr_count:     0
    .args:
      - .address_space:  global
        .offset:         0
        .size:           8
        .value_kind:     global_buffer
      - .address_space:  global
        .offset:         8
        .size:           8
        .value_kind:     global_buffer
      - .actual_access:  write_only
        .address_space:  global
        .offset:         16
        .size:           8
        .value_kind:     global_buffer
      - .actual_access:  read_only
        .address_space:  global
        .offset:         24
        .size:           8
        .value_kind:     global_buffer
      - .actual_access:  read_only
        .address_space:  global
        .offset:         32
        .size:           8
        .value_kind:     global_buffer
      - .actual_access:  read_only
        .address_space:  global
        .offset:         40
        .size:           8
        .value_kind:     global_buffer
      - .actual_access:  read_only
        .address_space:  global
        .offset:         48
        .size:           8
        .value_kind:     global_buffer
    .group_segment_fixed_size: 0
    .kernarg_segment_align: 8
    .kernarg_segment_size: 56
    .language:       OpenCL C
    .language_version:
      - 2
      - 0
    .max_flat_workgroup_size: 512
    .name:           _Z8moe_gemmILi0EEvPKDF16_S1_PvPKyPKiPKfS1_
    .private_segment_fixed_size: 0
    .sgpr_count:     98
    .sgpr_spill_count: 0
    .symbol:         _Z8moe_gemmILi0EEvPKDF16_S1_PvPKyPKiPKfS1_.kd
    .uniform_work_group_size: 1
    .uses_dynamic_stack: false
    .vgpr_count:     256
    .vgpr_spill_count: 0
    .wavefront_size: 64
  - .agpr_count:     0
    .args:
      - .address_space:  global
        .offset:         0
        .size:           8
        .value_kind:     global_buffer
      - .address_space:  global
        .offset:         8
        .size:           8
        .value_kind:     global_buffer
      - .actual_access:  write_only
        .address_space:  global
        .offset:         16
        .size:           8
        .value_kind:     global_buffer
      - .actual_access:  read_only
        .address_space:  global
        .offset:         24
        .size:           8
        .value_kind:     global_buffer
      - .actual_access:  read_only
        .address_space:  global
        .offset:         32
        .size:           8
        .value_kind:     global_buffer
      - .actual_access:  read_only
        .address_space:  global
        .offset:         40
        .size:           8
        .value_kind:     global_buffer
      - .actual_access:  read_only
        .address_space:  global
        .offset:         48
        .size:           8
        .value_kind:     global_buffer
    .group_segment_fixed_size: 0
    .kernarg_segment_align: 8
    .kernarg_segment_size: 56
    .language:       OpenCL C
    .language_version:
      - 2
      - 0
    .max_flat_workgroup_size: 512
    .name:           _Z8moe_gemmILi1EEvPKDF16_S1_PvPKyPKiPKfS1_
    .private_segment_fixed_size: 0
    .sgpr_count:     100
    .sgpr_spill_count: 0
    .symbol:         _Z8moe_gemmILi1EEvPKDF16_S1_PvPKyPKiPKfS1_.kd
    .uniform_work_group_size: 1
    .uses_dynamic_stack: false
    .vgpr_count:     184
    .vgpr_spill_count: 0
    .wavefront_size: 64
  - .agpr_count:     0
    .args:
      - .address_space:  global
        .offset:         0
        .size:           8
        .value_kind:     global_buffer
      - .address_space:  global
        .offset:         8
        .size:           8
        .value_kind:     global_buffer
      - .actual_access:  write_only
        .address_space:  global
        .offset:         16
        .size:           8
        .value_kind:     global_buffer
      - .actual_access:  read_only
        .address_space:  global
        .offset:         24
        .size:           8
        .value_kind:     global_buffer
      - .actual_access:  read_only
        .address_space:  global
        .offset:         32
        .size:           8
        .value_kind:     global_buffer
      - .actual_access:  read_only
        .address_space:  global
        .offset:         40
        .size:           8
        .value_kind:     global_buffer
      - .actual_access:  read_only
        .address_space:  global
        .offset:         48
        .size:           8
        .value_kind:     global_buffer
    .group_segment_fixed_size: 0
    .kernarg_segment_align: 8
    .kernarg_segment_size: 56
    .language:       OpenCL C
    .language_version:
      - 2
      - 0
    .max_flat_workgroup_size: 512
    .name:           _Z8moe_gemmILi2EEvPKDF16_S1_PvPKyPKiPKfS1_
    .private_segment_fixed_size: 0
    .sgpr_count:     100
    .sgpr_spill_count: 0
    .symbol:         _Z8moe_gemmILi2EEvPKDF16_S1_PvPKyPKiPKfS1_.kd
    .uniform_work_group_size: 1
    .uses_dynamic_stack: false
    .vgpr_count:     192
    .vgpr_spill_count: 0
    .wavefront_size: 64
